# second sub-tile row sum on two alternating partial sums; ALiBi k-step A operand in a per-unit zeroed register quad
# speedup vs baseline: 1.0004x; 1.0004x over previous
.LBB0_507:
	s_ashr_i32 s19, s19, 3
	s_andn2_b32 s19, s19, 31
	v_and_b32_e32 v99, 31, v4
	s_add_i32 s20, s19, s20
	v_or_b32_e32 v6, s20, v99
	v_ashrrev_i32_e32 v7, 31, v6
	s_and_b32 s18, s18, 3
	s_lshl_b32 s21, s21, 2
	v_lshl_add_u64 v[92:93], v[6:7], 0, s[82:83]
	v_mov_b64_e32 v[6:7], s[8:9]
	s_or_b32 s18, s18, s21
	v_mad_u64_u32 v[6:7], s[22:23], v92, s70, v[6:7]
	v_bfe_u32 v98, v4, 5, 1
	v_mad_i32_i24 v7, v93, s70, v7
	s_lshl_b32 s82, s18, 7
	v_lshl_add_u64 v[6:7], v[6:7], 0, s[82:83]
	v_lshlrev_b32_e32 v2, 4, v98
	v_lshl_add_u64 v[6:7], v[6:7], 0, v[2:3]
	s_mov_b64 s[22:23], 0x1200
	s_movk_i32 s21, 0x1000
	v_lshl_add_u64 v[124:125], v[6:7], 0, s[22:23]
	v_add_co_u32_e32 v6, vcc, s21, v6
	s_cmp_lt_i32 s17, 0
	s_nop 0
	v_addc_co_u32_e32 v7, vcc, 0, v7, vcc
	global_load_dwordx4 v[66:69], v[124:125], off offset:32
	global_load_dwordx4 v[70:73], v[124:125], off offset:64
	global_load_dwordx4 v[74:77], v[6:7], off offset:512
	global_load_dwordx4 v[78:81], v[124:125], off offset:96
	s_waitcnt vmcnt(0)
	v_mov_b32_e32 v90, v122
	v_min_u32_e32 v91, 0xc00, v123
	v_mov_b32_e32 v247, 0
	v_mov_b32_e32 v248, 0
	v_mov_b32_e32 v249, 0
	s_mov_b32 s32, 0
	s_cmpk_gt_i32 s16, 0xbff
	s_cbranch_scc1 .Lpf_win_skip
	s_mul_hi_i32 s84, s16, 0x2aaaaaab
	s_lshr_b32 s84, s84, 4
	s_mul_i32 s85, s84, 0xffffffa0
	s_add_i32 s85, s85, s16
	v_readlane_b32 s87, v254, 7
	v_readlane_b32 s88, v253, 1
	v_readlane_b32 s89, v253, 2
	s_lshl_b32 s86, s16, 7
	s_and_b32 s86, s86, 0x380
	v_ashrrev_i32_e32 v238, 2, v0
	v_and_b32_e32 v238, -4, v238
	v_add_u32_e32 v238, s86, v238
	v_lshlrev_b32_e32 v240, 4, v0
	v_and_b32_e32 v240, 0xf0, v240
	s_lshl_b32 s87, s87, 5
	s_add_i32 s92, s84, s87
	s_mov_b32 s93, 0
	s_mov_b32 s32, 3
	s_cmp_gt_i32 s85, 63
	s_cbranch_scc1 .Lpf_win_w2
	s_load_dwordx2 s[90:91], s[88:89], 0xa0
	s_lshl_b64 s[92:93], s[92:93], 23
	v_lshlrev_b32_e32 v238, 13, v238
	s_lshl_b32 s86, s85, 4
	s_and_b32 s86, s86, 0xffffff80
	s_lshl_b32 s86, s86, 2
	v_add3_u32 v238, v238, v240, s86
	v_mov_b32_e32 v239, 0
	s_waitcnt lgkmcnt(0)
	s_add_u32 s90, s90, s92
	s_addc_u32 s91, s91, s93
	v_lshl_add_u64 v[238:239], s[90:91], 0, v[238:239]
	s_mov_b64 s[94:95], 0x2000
	v_lshl_add_u64 v[240:241], v[238:239], 0, s[94:95]
	global_load_dwordx4 v[126:129], v[240:241], off nt
	s_mov_b64 s[94:95], 0x4000
	v_lshl_add_u64 v[242:243], v[238:239], 0, s[94:95]
	global_load_dwordx4 v[130:133], v[242:243], off nt
	global_load_dwordx4 v[134:137], v[238:239], off nt
	global_load_dwordx4 v[138:141], v[238:239], off offset:256 nt
	s_mov_b64 s[94:95], 0x6000
	v_lshl_add_u64 v[240:241], v[238:239], 0, s[94:95]
	global_load_dwordx4 v[142:145], v[240:241], off nt
	s_mov_b64 s[94:95], 0x2000
	v_lshl_add_u64 v[242:243], v[238:239], 0, s[94:95]
	global_load_dwordx4 v[146:149], v[242:243], off offset:256 nt
	s_mov_b64 s[94:95], 0x4000
	v_lshl_add_u64 v[240:241], v[238:239], 0, s[94:95]
	global_load_dwordx4 v[168:171], v[240:241], off offset:256 nt
	s_mov_b64 s[94:95], 0x6000
	v_lshl_add_u64 v[242:243], v[238:239], 0, s[94:95]
	global_load_dwordx4 v[172:175], v[242:243], off offset:256 nt
	s_mov_b64 s[94:95], 0x1000
	v_lshl_add_u64 v[240:241], v[238:239], 0, s[94:95]
	global_load_dwordx4 v[176:179], v[240:241], off nt
	s_mov_b64 s[94:95], 0x3000
	v_lshl_add_u64 v[242:243], v[238:239], 0, s[94:95]
	global_load_dwordx4 v[206:209], v[242:243], off nt
	s_mov_b64 s[94:95], 0x5000
	v_lshl_add_u64 v[240:241], v[238:239], 0, s[94:95]
	global_load_dwordx4 v[210:213], v[240:241], off nt
	s_mov_b64 s[94:95], 0x7000
	v_lshl_add_u64 v[242:243], v[238:239], 0, s[94:95]
	global_load_dwordx4 v[214:217], v[242:243], off nt
	s_mov_b64 s[94:95], 0x1000
	v_lshl_add_u64 v[240:241], v[238:239], 0, s[94:95]
	global_load_dwordx4 v[222:225], v[240:241], off offset:256 nt
	s_mov_b64 s[94:95], 0x3000
	v_lshl_add_u64 v[242:243], v[238:239], 0, s[94:95]
	global_load_dwordx4 v[226:229], v[242:243], off offset:256 nt
	s_mov_b64 s[94:95], 0x5000
	v_lshl_add_u64 v[240:241], v[238:239], 0, s[94:95]
	global_load_dwordx4 v[230:233], v[240:241], off offset:256 nt
	s_mov_b64 s[94:95], 0x7000
	v_lshl_add_u64 v[242:243], v[238:239], 0, s[94:95]
	global_load_dwordx4 v[234:237], v[242:243], off offset:256 nt
	s_branch .Lpf_win_skip

.LBB0_509:
	v_mul_f32_e32 v2, 0xbfb8aa3b, v110
	v_fmamk_f32 v16, v50, 0x3fb8aa3b, v2
	v_fmamk_f32 v50, v52, 0x3fb8aa3b, v2
	v_exp_f32_e32 v52, v50
	v_fmamk_f32 v50, v53, 0x3fb8aa3b, v2
	v_exp_f32_e32 v53, v50
	v_fmamk_f32 v50, v54, 0x3fb8aa3b, v2
	v_exp_f32_e32 v54, v50
	v_fmamk_f32 v50, v55, 0x3fb8aa3b, v2
	v_exp_f32_e32 v55, v50
	v_fmamk_f32 v50, v56, 0x3fb8aa3b, v2
	v_exp_f32_e32 v56, v50
	v_fmamk_f32 v50, v57, 0x3fb8aa3b, v2
	v_exp_f32_e32 v57, v50
	v_fmamk_f32 v50, v58, 0x3fb8aa3b, v2
	v_exp_f32_e32 v58, v50
	v_fmamk_f32 v50, v59, 0x3fb8aa3b, v2
	v_fmamk_f32 v17, v51, 0x3fb8aa3b, v2
	v_exp_f32_e32 v59, v50
	v_fmamk_f32 v50, v60, 0x3fb8aa3b, v2
	v_exp_f32_e32 v16, v16
	v_exp_f32_e32 v17, v17
	v_exp_f32_e32 v60, v50
	v_fmamk_f32 v50, v61, 0x3fb8aa3b, v2
	v_exp_f32_e32 v61, v50
	v_fmamk_f32 v50, v62, 0x3fb8aa3b, v2
	v_exp_f32_e32 v62, v50
	v_fmamk_f32 v50, v63, 0x3fb8aa3b, v2
	v_exp_f32_e32 v63, v50
	v_fmamk_f32 v50, v64, 0x3fb8aa3b, v2
	v_exp_f32_e32 v64, v50
	v_fmac_f32_e32 v2, 0x3fb8aa3b, v65
	v_pk_add_f32 v[50:51], v[16:17], v[52:53]
	v_exp_f32_e32 v65, v2
	v_pk_add_f32 v[244:245], v[54:55], v[56:57]
	v_pk_add_f32 v[50:51], v[58:59], v[50:51]
	v_pk_add_f32 v[244:245], v[60:61], v[244:245]
	v_pk_add_f32 v[50:51], v[62:63], v[50:51]
	v_pk_add_f32 v[244:245], v[64:65], v[244:245]
	s_nop 0
	v_pk_add_f32 v[50:51], v[50:51], v[244:245]
	s_nop 0
	v_add_f32_e32 v2, v50, v51
	v_cvt_pk_bf16_f32 v50, v16, v17
	v_cvt_pk_bf16_f32 v51, v52, v53
	v_cvt_pk_bf16_f32 v52, v54, v55
	v_cvt_pk_bf16_f32 v53, v56, v57
	v_add_f32_e32 v107, v107, v2
	s_waitcnt lgkmcnt(0)
	v_mfma_f32_32x32x16_bf16 v[34:49], v[86:89], v[50:53], v[34:49]
	v_mfma_f32_32x32x16_bf16 v[18:33], v[12:15], v[50:53], v[18:33]
	v_cvt_pk_bf16_f32 v12, v58, v59
	v_cvt_pk_bf16_f32 v13, v60, v61
	v_cvt_pk_bf16_f32 v14, v62, v63
	v_cvt_pk_bf16_f32 v15, v64, v65
	s_nop 0
	v_mfma_f32_32x32x16_bf16 v[34:49], v[8:11], v[12:15], v[34:49]
	v_mfma_f32_32x32x16_bf16 v[18:33], v[4:7], v[12:15], v[18:33]

.LBB0_521:
	s_add_i32 s3, s27, s21
	s_add_i32 s3, s3, -1
	s_and_b32 s31, s30, 0xc000
	s_add_i32 s33, s31, 0
	s_ashr_i32 s3, s3, 2
	s_add_i32 s31, s2, 0x7e0
	s_cmp_gt_i32 s31, s23
	v_cvt_f32_i32_e32 v111, s3
	s_cselect_b64 s[34:35], -1, 0
	s_add_i32 s3, s2, 0x7ff
	s_cmp_lt_i32 s3, s24
	s_cselect_b64 s[38:39], -1, 0
	v_add_u32_e32 v2, s33, v101
	v_add_u32_e32 v4, s33, v102
	v_add_u32_e32 v5, s33, v103
	v_add_u32_e32 v6, s33, v104
	s_or_b64 s[34:35], s[34:35], s[38:39]
	s_and_b64 vcc, exec, s[34:35]
	v_add_u32_e32 v115, v2, v100
	v_add_u32_e32 v114, v4, v100
	v_add_u32_e32 v113, v5, v100
	v_add_u32_e32 v112, v6, v100
	v_add_u32_e32 v16, s33, v105
	v_add_u32_e32 v17, s33, v106
	s_cbranch_vccnz .LBB0_527
	ds_read_b128 v[4:7], v115 offset:4096
	ds_read_b128 v[188:191], v114 offset:4096
	ds_read_b128 v[192:195], v113 offset:4096
	ds_read_b128 v[202:205], v112 offset:4096
	s_and_b32 s31, s31, 0xe0
	v_or_b32_e32 v2, s31, v99
	v_cvt_f32_ubyte0_e32 v2, v2
	v_and_b32_e32 v2, 0x7fff0000, v2
	v_or_b32_sdwa v2, v2, v111 dst_sel:DWORD dst_unused:UNUSED_PAD src0_sel:DWORD src1_sel:WORD_1
	v_cndmask_b32_e64 v246, 0, v2, s[36:37]
	s_cmp_ge_i32 s20, s3
	s_cselect_b64 s[34:35], -1, 0
	s_waitcnt lgkmcnt(3)
	v_mfma_f32_32x32x16_bf16 v[50:65], v[4:7], v[74:77], 0
	s_sub_i32 s3, s19, 32
	s_cmpk_lt_i32 s3, 0x1e1
	v_add3_u32 v116, v17, v94, s69
	s_cselect_b64 s[38:39], -1, 0
	s_and_b64 s[34:35], s[34:35], s[38:39]
	s_and_b64 vcc, exec, s[34:35]
	s_waitcnt lgkmcnt(2)
	v_mfma_f32_32x32x16_bf16 v[50:65], v[188:191], v[66:69], v[50:65]
	s_waitcnt lgkmcnt(1)
	v_mfma_f32_32x32x16_bf16 v[50:65], v[192:195], v[70:73], v[50:65]
	s_waitcnt lgkmcnt(0)
	v_mfma_f32_32x32x16_bf16 v[50:65], v[202:205], v[78:81], v[50:65]
	v_mfma_f32_32x32x16_bf16 v[50:65], v[246:249], v[82:85], v[50:65]
	v_add3_u32 v2, v16, v94, s69
	ds_read_b64_tr_b16 v[86:87], v2
	ds_read_b64_tr_b16 v[88:89], v2 offset:1024
	ds_read_b64_tr_b16 v[12:13], v116
	ds_read_b64_tr_b16 v[14:15], v116 offset:1024
	ds_read_b64_tr_b16 v[8:9], v2 offset:2048
	ds_read_b64_tr_b16 v[10:11], v2 offset:3072
	ds_read_b64_tr_b16 v[4:5], v116 offset:2048
	ds_read_b64_tr_b16 v[6:7], v116 offset:3072
	s_cbranch_vccnz .LBB0_524
	v_add_u32_e32 v2, s19, v108
	v_subrev_u32_e32 v116, 32, v2
	v_cmp_gt_u32_e32 vcc, s79, v116
	v_add3_u32 v116, v109, s22, 32
	s_nop 5
	v_cndmask_b32_e32 v50, v197, v50, vcc
	v_cmp_lt_u32_e32 vcc, s80, v116
	v_subrev_u32_e32 v116, 34, v2
	s_nop 0
	v_cndmask_b32_e32 v51, v197, v51, vcc
	v_cmp_gt_u32_e32 vcc, s79, v116
	v_subrev_u32_e32 v116, 35, v2
	s_nop 0
	v_cndmask_b32_e32 v52, v197, v52, vcc
	v_cmp_gt_u32_e32 vcc, s79, v116
	v_subrev_u32_e32 v116, 40, v2
	s_nop 0
	v_cndmask_b32_e32 v53, v197, v53, vcc
	v_cmp_gt_u32_e32 vcc, s79, v116
	v_subrev_u32_e32 v116, 41, v2
	s_nop 0
	v_cndmask_b32_e32 v54, v197, v54, vcc
	v_cmp_gt_u32_e32 vcc, s79, v116
	v_subrev_u32_e32 v116, 42, v2
	s_nop 0
	v_cndmask_b32_e32 v55, v197, v55, vcc
	v_cmp_gt_u32_e32 vcc, s79, v116
	v_subrev_u32_e32 v116, 43, v2
	s_nop 0
	v_cndmask_b32_e32 v56, v197, v56, vcc
	v_cmp_gt_u32_e32 vcc, s79, v116
	v_subrev_u32_e32 v116, 48, v2
	s_nop 0
	v_cndmask_b32_e32 v57, v197, v57, vcc
	v_cmp_gt_u32_e32 vcc, s79, v116
	v_subrev_u32_e32 v116, 49, v2
	s_nop 0
	v_cndmask_b32_e32 v58, v197, v58, vcc
	v_cmp_gt_u32_e32 vcc, s79, v116
	v_subrev_u32_e32 v116, 50, v2
	s_nop 0
	v_cndmask_b32_e32 v59, v197, v59, vcc
	v_cmp_gt_u32_e32 vcc, s79, v116
	v_subrev_u32_e32 v116, 51, v2
	s_nop 0
	v_cndmask_b32_e32 v60, v197, v60, vcc
	v_cmp_gt_u32_e32 vcc, s79, v116
	v_subrev_u32_e32 v116, 56, v2
	s_nop 0
	v_cndmask_b32_e32 v61, v197, v61, vcc
	v_cmp_gt_u32_e32 vcc, s79, v116
	v_subrev_u32_e32 v116, 57, v2
	s_nop 0
	v_cndmask_b32_e32 v62, v197, v62, vcc
	v_cmp_gt_u32_e32 vcc, s79, v116
	v_subrev_u32_e32 v116, 58, v2
	v_subrev_u32_e32 v2, 59, v2
	v_cndmask_b32_e32 v63, v197, v63, vcc
	v_cmp_gt_u32_e32 vcc, s79, v116
	s_nop 1
	v_cndmask_b32_e32 v64, v197, v64, vcc
	v_cmp_gt_u32_e32 vcc, s79, v2
	s_nop 1
	v_cndmask_b32_e32 v65, v197, v65, vcc

.LBB0_527:
	s_add_i32 s3, s2, 0x7c0
	s_cmp_gt_i32 s3, s23
	s_cselect_b64 s[34:35], -1, 0
	s_addk_i32 s2, 0x7df
	s_cmp_lt_i32 s2, s24
	s_cselect_b64 s[38:39], -1, 0
	s_or_b64 s[34:35], s[34:35], s[38:39]
	s_and_b64 vcc, exec, s[34:35]
	s_cbranch_vccnz .LBB0_510
	ds_read_b128 v[4:7], v115
	ds_read_b128 v[188:191], v114
	ds_read_b128 v[192:195], v113
	ds_read_b128 v[202:205], v112
	s_and_b32 s3, s3, 0xc0
	v_or_b32_e32 v2, s3, v99
	v_cvt_f32_ubyte0_e32 v2, v2
	v_and_b32_e32 v2, 0x7fff0000, v2
	v_or_b32_sdwa v2, v2, v111 dst_sel:DWORD dst_unused:UNUSED_PAD src0_sel:DWORD src1_sel:WORD_1
	v_cndmask_b32_e64 v246, 0, v2, s[36:37]
	s_cmp_ge_i32 s20, s2
	s_cselect_b64 s[2:3], -1, 0
	s_waitcnt lgkmcnt(3)
	v_mfma_f32_32x32x16_bf16 v[50:65], v[4:7], v[74:77], 0
	s_cmpk_lt_i32 s19, 0x1e1
	s_cselect_b64 s[34:35], -1, 0
	s_and_b64 s[2:3], s[2:3], s[34:35]
	s_and_b64 vcc, exec, s[2:3]
	s_waitcnt lgkmcnt(2)
	v_mfma_f32_32x32x16_bf16 v[50:65], v[188:191], v[66:69], v[50:65]
	s_waitcnt lgkmcnt(1)
	v_mfma_f32_32x32x16_bf16 v[50:65], v[192:195], v[70:73], v[50:65]
	s_waitcnt lgkmcnt(0)
	v_mfma_f32_32x32x16_bf16 v[50:65], v[202:205], v[78:81], v[50:65]
	v_mfma_f32_32x32x16_bf16 v[50:65], v[246:249], v[82:85], v[50:65]
	v_add3_u32 v2, v16, v94, s67
	v_add3_u32 v16, v17, v94, s67
	ds_read_b64_tr_b16 v[86:87], v2
	ds_read_b64_tr_b16 v[88:89], v2 offset:1024
	ds_read_b64_tr_b16 v[12:13], v16
	ds_read_b64_tr_b16 v[14:15], v16 offset:1024
	ds_read_b64_tr_b16 v[8:9], v2 offset:2048
	ds_read_b64_tr_b16 v[10:11], v2 offset:3072
	ds_read_b64_tr_b16 v[4:5], v16 offset:2048
	ds_read_b64_tr_b16 v[6:7], v16 offset:3072
	s_cbranch_vccnz .LBB0_530
	v_add_u32_e32 v2, s19, v108
	v_cmp_gt_u32_e32 vcc, s79, v2
	v_add_u32_e32 v16, s22, v109
	s_nop 5
	v_cndmask_b32_e32 v50, v197, v50, vcc
	v_cmp_lt_u32_e32 vcc, s80, v16
	v_add_u32_e32 v16, -2, v2
	s_nop 0
	v_cndmask_b32_e32 v51, v197, v51, vcc
	v_cmp_gt_u32_e32 vcc, s79, v16
	v_add_u32_e32 v16, -3, v2
	s_nop 0
	v_cndmask_b32_e32 v52, v197, v52, vcc
	v_cmp_gt_u32_e32 vcc, s79, v16
	v_add_u32_e32 v16, -8, v2
	s_nop 0
	v_cndmask_b32_e32 v53, v197, v53, vcc
	v_cmp_gt_u32_e32 vcc, s79, v16
	v_add_u32_e32 v16, -9, v2
	s_nop 0
	v_cndmask_b32_e32 v54, v197, v54, vcc
	v_cmp_gt_u32_e32 vcc, s79, v16
	v_add_u32_e32 v16, -10, v2
	s_nop 0
	v_cndmask_b32_e32 v55, v197, v55, vcc
	v_cmp_gt_u32_e32 vcc, s79, v16
	v_add_u32_e32 v16, -11, v2
	s_nop 0
	v_cndmask_b32_e32 v56, v197, v56, vcc
	v_cmp_gt_u32_e32 vcc, s79, v16
	v_add_u32_e32 v16, -16, v2
	s_nop 0
	v_cndmask_b32_e32 v57, v197, v57, vcc
	v_cmp_gt_u32_e32 vcc, s79, v16
	v_subrev_u32_e32 v16, 17, v2
	s_nop 0
	v_cndmask_b32_e32 v58, v197, v58, vcc
	v_cmp_gt_u32_e32 vcc, s79, v16
	v_subrev_u32_e32 v16, 18, v2
	s_nop 0
	v_cndmask_b32_e32 v59, v197, v59, vcc
	v_cmp_gt_u32_e32 vcc, s79, v16
	v_subrev_u32_e32 v16, 19, v2
	s_nop 0
	v_cndmask_b32_e32 v60, v197, v60, vcc
	v_cmp_gt_u32_e32 vcc, s79, v16
	v_subrev_u32_e32 v16, 24, v2
	s_nop 0
	v_cndmask_b32_e32 v61, v197, v61, vcc
	v_cmp_gt_u32_e32 vcc, s79, v16
	v_subrev_u32_e32 v16, 25, v2
	s_nop 0
	v_cndmask_b32_e32 v62, v197, v62, vcc
	v_cmp_gt_u32_e32 vcc, s79, v16
	v_subrev_u32_e32 v16, 26, v2
	v_subrev_u32_e32 v2, 27, v2
	v_cndmask_b32_e32 v63, v197, v63, vcc
	v_cmp_gt_u32_e32 vcc, s79, v16
	s_nop 1
	v_cndmask_b32_e32 v64, v197, v64, vcc
	v_cmp_gt_u32_e32 vcc, s79, v2
	s_nop 1
	v_cndmask_b32_e32 v65, v197, v65, vcc

.LBB0_661:
	v_readlane_b32 s0, v255, 26
	s_lshl_b32 s0, s0, 2
	v_readlane_b32 s8, v254, 44
	v_readlane_b32 s1, v254, 0
	s_add_i32 s0, s0, 0
	v_readlane_b32 s9, v254, 45
	v_mov_b32_e32 v2, s1
	v_lshl_add_u32 v11, v129, 2, s0
	s_and_b64 s[0:1], exec, s[8:9]
	s_waitcnt lgkmcnt(0)
	s_barrier
	ds_read_b32 v2, v2
	v_readlane_b32 s0, v254, 59
	s_cselect_b32 s4, 1, 2
	s_lshr_b32 s3, 0x80000000, s0
	v_readlane_b32 s0, v254, 46
	v_add_u32_e32 v11, 0x18800, v11
	s_lshl_b32 s5, 1, s0
	ds_read_b32 v136, v11
	v_mov_b32_e32 v211, 0
	v_mov_b32_e32 v212, 0
	v_mov_b32_e32 v213, 0
	s_and_b64 s[0:1], exec, s[8:9]
	s_cselect_b32 s0, 0, s5
	s_waitcnt lgkmcnt(1)
	v_readfirstlane_b32 s2, v2
	s_or_b32 s0, s0, s3
	s_andn2_b32 s0, s2, s0
	s_cmp_eq_u32 s0, 0
	s_mov_b32 s3, 0
	s_mov_b32 s76, 0x41000000
	v_readlane_b32 s16, v255, 33
	s_cbranch_scc1 .LBB0_665
	s_flbit_i32_b32 s1, s0
	s_xor_b32 s1, s1, 31
	s_lshl_b32 s3, 1, s1
	s_andn2_b32 s3, s0, s3
	s_mul_i32 s5, s1, 0xd8000
	v_readlane_b32 s17, v255, 32
	s_add_u32 s0, s17, s5
	v_readlane_b32 s18, v255, 31
	s_addc_u32 s1, s18, 0
	v_readlane_b32 s19, v255, 30
	s_add_u32 s6, s19, s5
	v_readlane_b32 s20, v255, 29
	s_addc_u32 s7, s20, 0
	s_lshl_b32 s5, s4, 14
	s_xor_b32 s5, s5, 0x8000
	s_add_i32 s5, s5, 0
	v_add_u32_e32 v11, s5, v66
	v_mov_b32_e32 v2, v132
	v_readfirstlane_b32 s5, v11
	s_mov_b32 m0, s5
	v_add_u32_e32 v11, 0x2000, v11
	s_cmp_lg_u32 s3, 0
	global_load_lds_dwordx4 v2, s[0:1]
	v_readfirstlane_b32 s0, v11
	v_mov_b32_e32 v2, v133
	s_mov_b32 m0, s0
	s_cselect_b64 s[0:1], -1, 0
	global_load_lds_dwordx4 v2, s[6:7]
	s_and_b64 s[0:1], s[8:9], s[0:1]
	v_readlane_b32 s64, v254, 9
	v_readlane_b32 s82, v255, 36
	v_readlane_b32 s48, v254, 40
	v_readlane_b32 s50, v254, 42
	v_readlane_b32 s22, v255, 27
	s_and_b64 vcc, exec, s[0:1]
	v_readlane_b32 s65, v254, 10
	v_readlane_b32 s66, v254, 15
	s_movk_i32 s67, 0x2000
	s_movk_i32 s68, 0x6000
	s_movk_i32 s69, 0x3000
	s_movk_i32 s70, 0x3600
	s_movk_i32 s71, 0x80
	s_movk_i32 s72, 0x70
	v_readlane_b32 s73, v254, 11
	s_movk_i32 s74, 0x1ff
	s_brev_b32 s75, -3
	s_mov_b32 s78, 0xc3e00000
	s_movk_i32 s79, 0x200
	s_movk_i32 s80, 0xfdff
	v_readlane_b32 s83, v255, 37
	v_readlane_b32 s49, v254, 41
	v_readlane_b32 s51, v254, 43
	v_readlane_b32 s14, v255, 34
	v_readlane_b32 s15, v255, 35
	v_readlane_b32 s23, v255, 28
	s_cbranch_vccz .LBB0_664
	s_flbit_i32_b32 s0, s3
	s_xor_b32 s6, s0, 31
	s_mul_i32 s4, s6, 0xd8000
	s_add_u32 s0, s17, s4
	v_readfirstlane_b32 s7, v127
	s_addc_u32 s1, s18, 0
	v_mov_b32_e32 v2, v132
	s_mov_b32 m0, s7
	s_add_u32 s4, s19, s4
	s_addc_u32 s5, s20, 0
	global_load_lds_dwordx4 v2, s[0:1]
	v_readfirstlane_b32 s0, v64
	v_mov_b32_e32 v2, v133
	s_mov_b32 m0, s0
	s_lshl_b32 s0, 1, s6
	global_load_lds_dwordx4 v2, s[4:5]
	s_andn2_b32 s3, s3, s0
	s_mov_b32 s4, 2

.LBB0_668:
	v_mul_f32_e32 v2, 0xbfb8aa3b, v158
	v_fmamk_f32 v16, v82, 0x3fb8aa3b, v2
	v_fmamk_f32 v82, v84, 0x3fb8aa3b, v2
	v_exp_f32_e32 v84, v82
	v_fmamk_f32 v82, v85, 0x3fb8aa3b, v2
	v_exp_f32_e32 v85, v82
	v_fmamk_f32 v82, v86, 0x3fb8aa3b, v2
	v_exp_f32_e32 v86, v82
	v_fmamk_f32 v82, v87, 0x3fb8aa3b, v2
	v_exp_f32_e32 v87, v82
	v_fmamk_f32 v82, v88, 0x3fb8aa3b, v2
	v_exp_f32_e32 v88, v82
	v_fmamk_f32 v82, v89, 0x3fb8aa3b, v2
	v_exp_f32_e32 v89, v82
	v_fmamk_f32 v82, v90, 0x3fb8aa3b, v2
	v_exp_f32_e32 v90, v82
	v_fmamk_f32 v82, v91, 0x3fb8aa3b, v2
	v_fmamk_f32 v17, v83, 0x3fb8aa3b, v2
	v_exp_f32_e32 v91, v82
	v_fmamk_f32 v82, v92, 0x3fb8aa3b, v2
	v_exp_f32_e32 v16, v16
	v_exp_f32_e32 v17, v17
	v_exp_f32_e32 v92, v82
	v_fmamk_f32 v82, v93, 0x3fb8aa3b, v2
	v_exp_f32_e32 v93, v82
	v_fmamk_f32 v82, v94, 0x3fb8aa3b, v2
	v_exp_f32_e32 v94, v82
	v_fmamk_f32 v82, v95, 0x3fb8aa3b, v2
	v_exp_f32_e32 v95, v82
	v_fmamk_f32 v82, v96, 0x3fb8aa3b, v2
	v_exp_f32_e32 v96, v82
	v_fmac_f32_e32 v2, 0x3fb8aa3b, v97
	v_pk_add_f32 v[82:83], v[16:17], v[84:85]
	v_exp_f32_e32 v97, v2
	v_pk_add_f32 v[218:219], v[86:87], v[88:89]
	v_pk_add_f32 v[82:83], v[90:91], v[82:83]
	v_pk_add_f32 v[218:219], v[92:93], v[218:219]
	v_pk_add_f32 v[82:83], v[94:95], v[82:83]
	v_pk_add_f32 v[218:219], v[96:97], v[218:219]
	s_nop 0
	v_pk_add_f32 v[82:83], v[82:83], v[218:219]
	s_nop 0
	v_add_f32_e32 v2, v82, v83
	v_cvt_pk_bf16_f32 v82, v16, v17
	v_cvt_pk_bf16_f32 v83, v84, v85
	v_cvt_pk_bf16_f32 v84, v86, v87
	v_cvt_pk_bf16_f32 v85, v88, v89
	v_add_f32_e32 v144, v144, v2
	s_waitcnt lgkmcnt(0)
	v_mfma_f32_32x32x16_bf16 v[66:81], v[118:121], v[82:85], v[66:81]
	v_mfma_f32_32x32x16_bf16 v[50:65], v[12:15], v[82:85], v[50:65]
	v_cvt_pk_bf16_f32 v12, v90, v91
	v_cvt_pk_bf16_f32 v13, v92, v93
	v_cvt_pk_bf16_f32 v14, v94, v95
	v_cvt_pk_bf16_f32 v15, v96, v97
	s_nop 0
	v_mfma_f32_32x32x16_bf16 v[66:81], v[8:11], v[12:15], v[66:81]
	v_mfma_f32_32x32x16_bf16 v[50:65], v[4:7], v[12:15], v[50:65]

.LBB0_681:
	s_flbit_i32_b32 s0, s2
	s_xor_b32 s0, s0, 31
	s_lshl_b32 s8, 1, s0
	s_waitcnt lgkmcnt(0)
	v_and_b32_e32 v2, s8, v136
	v_cmp_ne_u32_e64 s[38:39], 0, v2
	s_mov_b64 vcc, s[38:39]
	s_cbranch_vccz .LBB0_669
	s_and_b32 s1, s5, 0xc000
	s_lshl_b32 s9, s0, 6
	s_lshr_b32 s0, s0, 2
	s_xor_b32 s1, s1, 0x8000
	v_cvt_f32_u32_e32 v159, s0
	s_add_i32 s1, s1, 0
	v_add_u32_e32 v2, s1, v137
	v_add_u32_e32 v4, s1, v138
	v_add_u32_e32 v5, s1, v139
	v_add_u32_e32 v6, s1, v140
	s_or_b32 s10, s9, 32
	s_cmp_gt_i32 s10, s6
	v_add_u32_e32 v163, v2, v134
	v_add_u32_e32 v162, v4, v134
	v_add_u32_e32 v161, v5, v134
	v_add_u32_e32 v160, v6, v134
	v_add_u32_e32 v17, s1, v156
	v_add_u32_e32 v16, s1, v157
	s_cbranch_scc1 .LBB0_690
	ds_read_b128 v[4:7], v163 offset:4096
	ds_read_b128 v[188:191], v162 offset:4096
	ds_read_b128 v[192:195], v161 offset:4096
	ds_read_b128 v[202:205], v160 offset:4096
	s_and_b32 s0, s10, 0xe0
	v_or_b32_e32 v2, s0, v129
	v_cvt_f32_ubyte0_e32 v2, v2
	v_and_b32_e32 v2, 0x7fff0000, v2
	v_or_b32_sdwa v2, v2, v159 dst_sel:DWORD dst_unused:UNUSED_PAD src0_sel:DWORD src1_sel:WORD_1
	v_cndmask_b32_e64 v210, 0, v2, s[22:23]
	s_or_b32 s0, s9, 63
	s_cmp_lt_u32 s16, s0
	s_waitcnt lgkmcnt(3)
	v_mfma_f32_32x32x16_bf16 v[82:97], v[4:7], v[106:109], 0
	s_cselect_b64 s[0:1], -1, 0
	s_sub_i32 s11, s16, s10
	s_cmp_gt_i32 s11, 0x3fffffe0
	v_add3_u32 v164, v16, v135, s69
	s_cselect_b64 s[12:13], -1, 0
	s_or_b64 s[0:1], s[0:1], s[12:13]
	s_and_b64 vcc, exec, s[0:1]
	s_waitcnt lgkmcnt(2)
	v_mfma_f32_32x32x16_bf16 v[82:97], v[188:191], v[98:101], v[82:97]
	s_waitcnt lgkmcnt(1)
	v_mfma_f32_32x32x16_bf16 v[82:97], v[192:195], v[102:105], v[82:97]
	s_waitcnt lgkmcnt(0)
	v_mfma_f32_32x32x16_bf16 v[82:97], v[202:205], v[110:113], v[82:97]
	v_mfma_f32_32x32x16_bf16 v[82:97], v[210:213], v[114:117], v[82:97]
	v_add3_u32 v2, v17, v135, s69
	ds_read_b64_tr_b16 v[118:119], v2
	ds_read_b64_tr_b16 v[120:121], v2 offset:1024
	ds_read_b64_tr_b16 v[12:13], v164
	ds_read_b64_tr_b16 v[14:15], v164 offset:1024
	ds_read_b64_tr_b16 v[8:9], v2 offset:2048
	ds_read_b64_tr_b16 v[10:11], v2 offset:3072
	ds_read_b64_tr_b16 v[4:5], v164 offset:2048
	ds_read_b64_tr_b16 v[6:7], v164 offset:3072
	s_cbranch_vccnz .LBB0_685
	v_cndmask_b32_e64 v2, 0, 1, s[38:39]
	v_cmp_ne_u32_e32 vcc, 0, v2
	s_cmp_lg_u64 vcc, exec
	s_cselect_b64 s[0:1], -1, 0
	s_cbranch_scc0 .LBB0_687
	v_cndmask_b32_e64 v82, v197, v82, s[38:39]
	v_cndmask_b32_e64 v83, v197, v83, s[38:39]
	v_cndmask_b32_e64 v84, v197, v84, s[38:39]
	v_cndmask_b32_e64 v85, v197, v85, s[38:39]
	v_cndmask_b32_e64 v86, v197, v86, s[38:39]
	v_cndmask_b32_e64 v87, v197, v87, s[38:39]
	v_cndmask_b32_e64 v88, v197, v88, s[38:39]
	v_cndmask_b32_e64 v89, v197, v89, s[38:39]
	v_cndmask_b32_e64 v90, v197, v90, s[38:39]
	v_cndmask_b32_e64 v91, v197, v91, s[38:39]
	v_cndmask_b32_e64 v92, v197, v92, s[38:39]
	v_cndmask_b32_e64 v93, v197, v93, s[38:39]
	v_cndmask_b32_e64 v94, v197, v94, s[38:39]
	v_cndmask_b32_e64 v95, v197, v95, s[38:39]
	v_cndmask_b32_e64 v96, v197, v96, s[38:39]
	v_cndmask_b32_e64 v97, v197, v97, s[38:39]
	s_branch .LBB0_687

.LBB0_690:
	s_cmp_gt_i32 s9, s6
	s_cbranch_scc1 .LBB0_669
	ds_read_b128 v[4:7], v163
	ds_read_b128 v[188:191], v162
	ds_read_b128 v[192:195], v161
	ds_read_b128 v[202:205], v160
	s_and_b32 s0, s9, 0xc0
	v_or_b32_e32 v2, s0, v129
	v_cvt_f32_ubyte0_e32 v2, v2
	v_and_b32_e32 v2, 0x7fff0000, v2
	v_or_b32_sdwa v2, v2, v159 dst_sel:DWORD dst_unused:UNUSED_PAD src0_sel:DWORD src1_sel:WORD_1
	v_cndmask_b32_e64 v210, 0, v2, s[22:23]
	s_or_b32 s0, s9, 31
	s_cmp_lt_i32 s16, s0
	s_waitcnt lgkmcnt(3)
	v_mfma_f32_32x32x16_bf16 v[82:97], v[4:7], v[106:109], 0
	s_cselect_b64 s[0:1], -1, 0
	s_sub_i32 s10, s16, s9
	s_cmp_gt_i32 s10, 0x3fffffe0
	v_add3_u32 v16, v16, v135, s67
	s_cselect_b64 s[10:11], -1, 0
	s_or_b64 s[0:1], s[0:1], s[10:11]
	s_and_b64 vcc, exec, s[0:1]
	s_waitcnt lgkmcnt(2)
	v_mfma_f32_32x32x16_bf16 v[82:97], v[188:191], v[98:101], v[82:97]
	s_waitcnt lgkmcnt(1)
	v_mfma_f32_32x32x16_bf16 v[82:97], v[192:195], v[102:105], v[82:97]
	s_waitcnt lgkmcnt(0)
	v_mfma_f32_32x32x16_bf16 v[82:97], v[202:205], v[110:113], v[82:97]
	v_mfma_f32_32x32x16_bf16 v[82:97], v[210:213], v[114:117], v[82:97]
	v_add3_u32 v2, v17, v135, s67
	ds_read_b64_tr_b16 v[118:119], v2
	ds_read_b64_tr_b16 v[120:121], v2 offset:1024
	ds_read_b64_tr_b16 v[12:13], v16
	ds_read_b64_tr_b16 v[14:15], v16 offset:1024
	ds_read_b64_tr_b16 v[8:9], v2 offset:2048
	ds_read_b64_tr_b16 v[10:11], v2 offset:3072
	ds_read_b64_tr_b16 v[4:5], v16 offset:2048
	ds_read_b64_tr_b16 v[6:7], v16 offset:3072
	s_cbranch_vccnz .LBB0_693
	v_cndmask_b32_e64 v2, 0, 1, s[38:39]
	v_cmp_ne_u32_e32 vcc, 0, v2
	s_cmp_lg_u64 vcc, exec
	s_cselect_b64 s[0:1], -1, 0
	s_cbranch_scc0 .LBB0_695
	v_cndmask_b32_e64 v82, v197, v82, s[38:39]
	v_cndmask_b32_e64 v83, v197, v83, s[38:39]
	v_cndmask_b32_e64 v84, v197, v84, s[38:39]
	v_cndmask_b32_e64 v85, v197, v85, s[38:39]
	v_cndmask_b32_e64 v86, v197, v86, s[38:39]
	v_cndmask_b32_e64 v87, v197, v87, s[38:39]
	v_cndmask_b32_e64 v88, v197, v88, s[38:39]
	v_cndmask_b32_e64 v89, v197, v89, s[38:39]
	v_cndmask_b32_e64 v90, v197, v90, s[38:39]
	v_cndmask_b32_e64 v91, v197, v91, s[38:39]
	v_cndmask_b32_e64 v92, v197, v92, s[38:39]
	v_cndmask_b32_e64 v93, v197, v93, s[38:39]
	v_cndmask_b32_e64 v94, v197, v94, s[38:39]
	v_cndmask_b32_e64 v95, v197, v95, s[38:39]
	v_cndmask_b32_e64 v96, v197, v96, s[38:39]
	v_cndmask_b32_e64 v97, v197, v97, s[38:39]
	s_branch .LBB0_695

.LBB0_768:
	s_and_b32 s14, s14, 3
	s_lshl_b32 s17, s17, 2
	s_or_b32 s14, s14, s17
	s_add_i32 s17, s14, 1
	v_cvt_f32_ubyte0_e32 v2, s17
	s_mov_b32 s17, 0x42fc0000
	v_cmp_lt_f32_e32 vcc, s17, v2
	v_mov_b32_e32 v5, 0x42800000
	s_ashr_i32 s15, s15, 3
	v_cndmask_b32_e32 v5, 0, v5, vcc
	s_andn2_b32 s15, s15, 31
	v_sub_f32_e32 v2, v5, v2
	v_and_b32_e32 v102, 31, v4
	s_add_i32 s16, s15, s16
	v_exp_f32_e32 v2, v2
	v_or_b32_e32 v94, s16, v102
	s_and_b64 s[18:19], vcc, exec
	v_ashrrev_i32_e32 v95, 31, v94
	s_cselect_b32 s18, 0xffffffc0, 0
	v_lshl_add_u64 v[92:93], v[94:95], 0, s[82:83]
	v_mov_b64_e32 v[6:7], s[50:51]
	v_ldexp_f32 v100, v2, s18
	v_mad_u64_u32 v[6:7], s[18:19], v92, s70, v[6:7]
	v_bfe_u32 v101, v4, 5, 1
	v_mad_i32_i24 v7, v93, s70, v7
	s_lshl_b32 s82, s14, 7
	v_lshl_add_u64 v[6:7], v[6:7], 0, s[82:83]
	v_lshlrev_b32_e32 v2, 4, v101
	v_lshl_add_u64 v[6:7], v[6:7], 0, v[2:3]
	global_load_dwordx4 v[66:69], v[6:7], off
	global_load_dwordx4 v[70:73], v[6:7], off offset:32
	global_load_dwordx4 v[74:77], v[6:7], off offset:64
	global_load_dwordx4 v[78:81], v[6:7], off offset:96
	s_load_dwordx2 s[18:19], s[48:49], 0x40
	s_or_b32 s82, s14, s33
	s_lshl_b64 s[20:21], s[82:83], 2
	s_mov_b32 s17, 0
	s_waitcnt lgkmcnt(0)
	s_add_u32 s18, s18, s20
	s_addc_u32 s19, s19, s21
	global_load_dword v95, v3, s[18:19]
	s_cmp_lt_i32 s13, 0
	s_waitcnt vmcnt(0)
	v_mov_b32_e32 v90, v122
	v_min_u32_e32 v91, 0xc00, v123
	v_mov_b32_e32 v247, 0
	v_mov_b32_e32 v248, 0
	v_mov_b32_e32 v249, 0
	s_mov_b32 s32, 0
	s_cmpk_gt_i32 s12, 0xbff
	s_cbranch_scc1 .Lpf_swa_skip
	s_mul_hi_i32 s84, s12, 0x2aaaaaab
	s_lshr_b32 s84, s84, 4
	s_mul_i32 s85, s84, 0xffffffa0
	s_add_i32 s85, s85, s12
	v_readlane_b32 s87, v254, 7
	v_readlane_b32 s88, v253, 1
	v_readlane_b32 s89, v253, 2
	s_lshl_b32 s86, s12, 7
	s_and_b32 s86, s86, 0x380
	v_ashrrev_i32_e32 v238, 2, v0
	v_and_b32_e32 v238, -4, v238
	v_add_u32_e32 v238, s86, v238
	v_lshlrev_b32_e32 v240, 4, v0
	v_and_b32_e32 v240, 0xf0, v240
	s_lshl_b32 s87, s87, 5
	s_add_i32 s92, s84, s87
	s_mov_b32 s93, 0
	s_mov_b32 s32, 3
	s_cmp_gt_i32 s85, 63
	s_cbranch_scc1 .Lpf_swa_w2
	s_load_dwordx2 s[90:91], s[88:89], 0xa0
	s_lshl_b64 s[92:93], s[92:93], 23
	v_lshlrev_b32_e32 v238, 13, v238
	s_lshl_b32 s86, s85, 4
	s_and_b32 s86, s86, 0xffffff80
	s_lshl_b32 s86, s86, 2
	v_add3_u32 v238, v238, v240, s86
	v_mov_b32_e32 v239, 0
	s_waitcnt lgkmcnt(0)
	s_add_u32 s90, s90, s92
	s_addc_u32 s91, s91, s93
	v_lshl_add_u64 v[238:239], s[90:91], 0, v[238:239]
	s_mov_b64 s[94:95], 0x2000
	v_lshl_add_u64 v[240:241], v[238:239], 0, s[94:95]
	global_load_dwordx4 v[126:129], v[240:241], off nt
	s_mov_b64 s[94:95], 0x4000
	v_lshl_add_u64 v[242:243], v[238:239], 0, s[94:95]
	global_load_dwordx4 v[130:133], v[242:243], off nt
	global_load_dwordx4 v[134:137], v[238:239], off nt
	global_load_dwordx4 v[138:141], v[238:239], off offset:256 nt
	s_mov_b64 s[94:95], 0x6000
	v_lshl_add_u64 v[240:241], v[238:239], 0, s[94:95]
	global_load_dwordx4 v[142:145], v[240:241], off nt
	s_mov_b64 s[94:95], 0x2000
	v_lshl_add_u64 v[242:243], v[238:239], 0, s[94:95]
	global_load_dwordx4 v[146:149], v[242:243], off offset:256 nt
	s_mov_b64 s[94:95], 0x4000
	v_lshl_add_u64 v[240:241], v[238:239], 0, s[94:95]
	global_load_dwordx4 v[168:171], v[240:241], off offset:256 nt
	s_mov_b64 s[94:95], 0x6000
	v_lshl_add_u64 v[242:243], v[238:239], 0, s[94:95]
	global_load_dwordx4 v[172:175], v[242:243], off offset:256 nt
	s_mov_b64 s[94:95], 0x1000
	v_lshl_add_u64 v[240:241], v[238:239], 0, s[94:95]
	global_load_dwordx4 v[176:179], v[240:241], off nt
	s_mov_b64 s[94:95], 0x3000
	v_lshl_add_u64 v[242:243], v[238:239], 0, s[94:95]
	global_load_dwordx4 v[206:209], v[242:243], off nt
	s_mov_b64 s[94:95], 0x5000
	v_lshl_add_u64 v[240:241], v[238:239], 0, s[94:95]
	global_load_dwordx4 v[210:213], v[240:241], off nt
	s_mov_b64 s[94:95], 0x7000
	v_lshl_add_u64 v[242:243], v[238:239], 0, s[94:95]
	global_load_dwordx4 v[214:217], v[242:243], off nt
	s_mov_b64 s[94:95], 0x1000
	v_lshl_add_u64 v[240:241], v[238:239], 0, s[94:95]
	global_load_dwordx4 v[222:225], v[240:241], off offset:256 nt
	s_mov_b64 s[94:95], 0x3000
	v_lshl_add_u64 v[242:243], v[238:239], 0, s[94:95]
	global_load_dwordx4 v[226:229], v[242:243], off offset:256 nt
	s_mov_b64 s[94:95], 0x5000
	v_lshl_add_u64 v[240:241], v[238:239], 0, s[94:95]
	global_load_dwordx4 v[230:233], v[240:241], off offset:256 nt
	s_mov_b64 s[94:95], 0x7000
	v_lshl_add_u64 v[242:243], v[238:239], 0, s[94:95]
	global_load_dwordx4 v[234:237], v[242:243], off offset:256 nt
	s_branch .Lpf_swa_skip

.LBB0_770:
	v_mul_f32_e32 v2, 0xbfb8aa3b, v113
	v_fmamk_f32 v16, v50, 0x3fb8aa3b, v2
	v_fmamk_f32 v50, v52, 0x3fb8aa3b, v2
	v_exp_f32_e32 v52, v50
	v_fmamk_f32 v50, v53, 0x3fb8aa3b, v2
	v_exp_f32_e32 v53, v50
	v_fmamk_f32 v50, v54, 0x3fb8aa3b, v2
	v_exp_f32_e32 v54, v50
	v_fmamk_f32 v50, v55, 0x3fb8aa3b, v2
	v_exp_f32_e32 v55, v50
	v_fmamk_f32 v50, v56, 0x3fb8aa3b, v2
	v_exp_f32_e32 v56, v50
	v_fmamk_f32 v50, v57, 0x3fb8aa3b, v2
	v_exp_f32_e32 v57, v50
	v_fmamk_f32 v50, v58, 0x3fb8aa3b, v2
	v_exp_f32_e32 v58, v50
	v_fmamk_f32 v50, v59, 0x3fb8aa3b, v2
	v_fmamk_f32 v17, v51, 0x3fb8aa3b, v2
	v_exp_f32_e32 v59, v50
	v_fmamk_f32 v50, v60, 0x3fb8aa3b, v2
	v_exp_f32_e32 v16, v16
	v_exp_f32_e32 v17, v17
	v_exp_f32_e32 v60, v50
	v_fmamk_f32 v50, v61, 0x3fb8aa3b, v2
	v_exp_f32_e32 v61, v50
	v_fmamk_f32 v50, v62, 0x3fb8aa3b, v2
	v_exp_f32_e32 v62, v50
	v_fmamk_f32 v50, v63, 0x3fb8aa3b, v2
	v_exp_f32_e32 v63, v50
	v_fmamk_f32 v50, v64, 0x3fb8aa3b, v2
	v_exp_f32_e32 v64, v50
	v_fmac_f32_e32 v2, 0x3fb8aa3b, v65
	v_pk_add_f32 v[50:51], v[16:17], v[52:53]
	v_exp_f32_e32 v65, v2
	v_pk_add_f32 v[244:245], v[54:55], v[56:57]
	v_pk_add_f32 v[50:51], v[58:59], v[50:51]
	v_pk_add_f32 v[244:245], v[60:61], v[244:245]
	v_pk_add_f32 v[50:51], v[62:63], v[50:51]
	v_pk_add_f32 v[244:245], v[64:65], v[244:245]
	s_nop 0
	v_pk_add_f32 v[50:51], v[50:51], v[244:245]
	s_nop 0
	v_add_f32_e32 v2, v50, v51
	v_cvt_pk_bf16_f32 v50, v16, v17
	v_cvt_pk_bf16_f32 v51, v52, v53
	v_cvt_pk_bf16_f32 v52, v54, v55
	v_cvt_pk_bf16_f32 v53, v56, v57
	v_add_f32_e32 v108, v108, v2
	s_waitcnt lgkmcnt(0)
	v_mfma_f32_32x32x16_bf16 v[34:49], v[86:89], v[50:53], v[34:49]
	v_mfma_f32_32x32x16_bf16 v[18:33], v[12:15], v[50:53], v[18:33]
	v_cvt_pk_bf16_f32 v12, v58, v59
	v_cvt_pk_bf16_f32 v13, v60, v61
	v_cvt_pk_bf16_f32 v14, v62, v63
	v_cvt_pk_bf16_f32 v15, v64, v65
	s_nop 0
	v_mfma_f32_32x32x16_bf16 v[34:49], v[8:11], v[12:15], v[34:49]
	v_mfma_f32_32x32x16_bf16 v[18:33], v[4:7], v[12:15], v[18:33]

.LBB0_782:
	s_add_i32 s1, s23, s18
	s_add_i32 s1, s1, -1
	s_and_b32 s27, s26, 0xc000
	s_add_i32 s34, s27, 0
	s_ashr_i32 s1, s1, 2
	s_add_i32 s27, s0, 0x7e0
	s_cmp_gt_i32 s27, s19
	v_cvt_f32_i32_e32 v114, s1
	s_cselect_b64 s[28:29], -1, 0
	s_add_i32 s1, s0, 0x7ff
	s_cmp_lt_i32 s1, s20
	s_cselect_b64 s[30:31], -1, 0
	v_add_u32_e32 v2, s34, v104
	v_add_u32_e32 v4, s34, v105
	v_add_u32_e32 v5, s34, v106
	v_add_u32_e32 v6, s34, v107
	s_or_b64 s[28:29], s[28:29], s[30:31]
	s_and_b64 vcc, exec, s[28:29]
	v_add_u32_e32 v118, v2, v103
	v_add_u32_e32 v117, v4, v103
	v_add_u32_e32 v116, v5, v103
	v_add_u32_e32 v115, v6, v103
	v_add_u32_e32 v16, s34, v109
	v_add_u32_e32 v17, s34, v110
	s_cbranch_vccnz .LBB0_788
	ds_read_b128 v[4:7], v118 offset:4096
	ds_read_b128 v[188:191], v117 offset:4096
	ds_read_b128 v[192:195], v116 offset:4096
	ds_read_b128 v[202:205], v115 offset:4096
	s_and_b32 s27, s27, 0xe0
	v_or_b32_e32 v2, s27, v102
	v_cvt_f32_ubyte0_e32 v2, v2
	v_and_b32_e32 v2, 0x7fff0000, v2
	v_or_b32_sdwa v2, v2, v114 dst_sel:DWORD dst_unused:UNUSED_PAD src0_sel:DWORD src1_sel:WORD_1
	v_cndmask_b32_e64 v246, 0, v2, s[36:37]
	s_cmp_ge_i32 s16, s1
	s_cselect_b64 s[28:29], -1, 0
	s_waitcnt lgkmcnt(3)
	v_mfma_f32_32x32x16_bf16 v[50:65], v[4:7], v[66:69], 0
	s_sub_i32 s1, s15, 32
	s_cmpk_lt_i32 s1, 0x61
	v_add3_u32 v119, v17, v96, s69
	s_cselect_b64 s[30:31], -1, 0
	s_and_b64 s[28:29], s[28:29], s[30:31]
	s_and_b64 vcc, exec, s[28:29]
	s_waitcnt lgkmcnt(2)
	v_mfma_f32_32x32x16_bf16 v[50:65], v[188:191], v[70:73], v[50:65]
	s_waitcnt lgkmcnt(1)
	v_mfma_f32_32x32x16_bf16 v[50:65], v[192:195], v[74:77], v[50:65]
	s_waitcnt lgkmcnt(0)
	v_mfma_f32_32x32x16_bf16 v[50:65], v[202:205], v[78:81], v[50:65]
	v_mfma_f32_32x32x16_bf16 v[50:65], v[246:249], v[82:85], v[50:65]
	v_add3_u32 v2, v16, v96, s69
	ds_read_b64_tr_b16 v[86:87], v2
	ds_read_b64_tr_b16 v[88:89], v2 offset:1024
	ds_read_b64_tr_b16 v[12:13], v119
	ds_read_b64_tr_b16 v[14:15], v119 offset:1024
	ds_read_b64_tr_b16 v[8:9], v2 offset:2048
	ds_read_b64_tr_b16 v[10:11], v2 offset:3072
	ds_read_b64_tr_b16 v[4:5], v119 offset:2048
	ds_read_b64_tr_b16 v[6:7], v119 offset:3072
	s_cbranch_vccnz .LBB0_785
	v_add_u32_e32 v2, s15, v111
	v_subrev_u32_e32 v119, 32, v2
	v_cmp_gt_u32_e32 vcc, s71, v119
	v_add3_u32 v119, v112, s17, 32
	s_nop 5
	v_cndmask_b32_e32 v50, v197, v50, vcc
	v_cmp_lt_u32_e32 vcc, s47, v119
	v_subrev_u32_e32 v119, 34, v2
	s_nop 0
	v_cndmask_b32_e32 v51, v197, v51, vcc
	v_cmp_gt_u32_e32 vcc, s71, v119
	v_subrev_u32_e32 v119, 35, v2
	s_nop 0
	v_cndmask_b32_e32 v52, v197, v52, vcc
	v_cmp_gt_u32_e32 vcc, s71, v119
	v_subrev_u32_e32 v119, 40, v2
	s_nop 0
	v_cndmask_b32_e32 v53, v197, v53, vcc
	v_cmp_gt_u32_e32 vcc, s71, v119
	v_subrev_u32_e32 v119, 41, v2
	s_nop 0
	v_cndmask_b32_e32 v54, v197, v54, vcc
	v_cmp_gt_u32_e32 vcc, s71, v119
	v_subrev_u32_e32 v119, 42, v2
	s_nop 0
	v_cndmask_b32_e32 v55, v197, v55, vcc
	v_cmp_gt_u32_e32 vcc, s71, v119
	v_subrev_u32_e32 v119, 43, v2
	s_nop 0
	v_cndmask_b32_e32 v56, v197, v56, vcc
	v_cmp_gt_u32_e32 vcc, s71, v119
	v_subrev_u32_e32 v119, 48, v2
	s_nop 0
	v_cndmask_b32_e32 v57, v197, v57, vcc
	v_cmp_gt_u32_e32 vcc, s71, v119
	v_subrev_u32_e32 v119, 49, v2
	s_nop 0
	v_cndmask_b32_e32 v58, v197, v58, vcc
	v_cmp_gt_u32_e32 vcc, s71, v119
	v_subrev_u32_e32 v119, 50, v2
	s_nop 0
	v_cndmask_b32_e32 v59, v197, v59, vcc
	v_cmp_gt_u32_e32 vcc, s71, v119
	v_subrev_u32_e32 v119, 51, v2
	s_nop 0
	v_cndmask_b32_e32 v60, v197, v60, vcc
	v_cmp_gt_u32_e32 vcc, s71, v119
	v_subrev_u32_e32 v119, 56, v2
	s_nop 0
	v_cndmask_b32_e32 v61, v197, v61, vcc
	v_cmp_gt_u32_e32 vcc, s71, v119
	v_subrev_u32_e32 v119, 57, v2
	s_nop 0
	v_cndmask_b32_e32 v62, v197, v62, vcc
	v_cmp_gt_u32_e32 vcc, s71, v119
	v_subrev_u32_e32 v119, 58, v2
	v_subrev_u32_e32 v2, 59, v2
	v_cndmask_b32_e32 v63, v197, v63, vcc
	v_cmp_gt_u32_e32 vcc, s71, v119
	s_nop 1
	v_cndmask_b32_e32 v64, v197, v64, vcc
	v_cmp_gt_u32_e32 vcc, s71, v2
	s_nop 1
	v_cndmask_b32_e32 v65, v197, v65, vcc

.LBB0_788:
	s_add_i32 s1, s0, 0x7c0
	s_cmp_gt_i32 s1, s19
	s_cselect_b64 s[28:29], -1, 0
	s_addk_i32 s0, 0x7df
	s_cmp_lt_i32 s0, s20
	s_cselect_b64 s[30:31], -1, 0
	s_or_b64 s[28:29], s[28:29], s[30:31]
	s_and_b64 vcc, exec, s[28:29]
	s_cbranch_vccnz .LBB0_771
	ds_read_b128 v[4:7], v118
	ds_read_b128 v[188:191], v117
	ds_read_b128 v[192:195], v116
	ds_read_b128 v[202:205], v115
	s_and_b32 s1, s1, 0xc0
	v_or_b32_e32 v2, s1, v102
	v_cvt_f32_ubyte0_e32 v2, v2
	v_and_b32_e32 v2, 0x7fff0000, v2
	v_or_b32_sdwa v2, v2, v114 dst_sel:DWORD dst_unused:UNUSED_PAD src0_sel:DWORD src1_sel:WORD_1
	v_cndmask_b32_e64 v246, 0, v2, s[36:37]
	s_cmp_ge_i32 s16, s0
	s_cselect_b64 s[0:1], -1, 0
	s_waitcnt lgkmcnt(3)
	v_mfma_f32_32x32x16_bf16 v[50:65], v[4:7], v[66:69], 0
	s_cmpk_lt_i32 s15, 0x61
	s_cselect_b64 s[28:29], -1, 0
	s_and_b64 s[0:1], s[0:1], s[28:29]
	s_and_b64 vcc, exec, s[0:1]
	s_waitcnt lgkmcnt(2)
	v_mfma_f32_32x32x16_bf16 v[50:65], v[188:191], v[70:73], v[50:65]
	s_waitcnt lgkmcnt(1)
	v_mfma_f32_32x32x16_bf16 v[50:65], v[192:195], v[74:77], v[50:65]
	s_waitcnt lgkmcnt(0)
	v_mfma_f32_32x32x16_bf16 v[50:65], v[202:205], v[78:81], v[50:65]
	v_mfma_f32_32x32x16_bf16 v[50:65], v[246:249], v[82:85], v[50:65]
	v_add3_u32 v2, v16, v96, s67
	v_add3_u32 v16, v17, v96, s67
	ds_read_b64_tr_b16 v[86:87], v2
	ds_read_b64_tr_b16 v[88:89], v2 offset:1024
	ds_read_b64_tr_b16 v[12:13], v16
	ds_read_b64_tr_b16 v[14:15], v16 offset:1024
	ds_read_b64_tr_b16 v[8:9], v2 offset:2048
	ds_read_b64_tr_b16 v[10:11], v2 offset:3072
	ds_read_b64_tr_b16 v[4:5], v16 offset:2048
	ds_read_b64_tr_b16 v[6:7], v16 offset:3072
	s_cbranch_vccnz .LBB0_791
	v_add_u32_e32 v2, s15, v111
	v_cmp_gt_u32_e32 vcc, s71, v2
	v_add_u32_e32 v16, s17, v112
	s_nop 5
	v_cndmask_b32_e32 v50, v197, v50, vcc
	v_cmp_lt_u32_e32 vcc, s47, v16
	v_add_u32_e32 v16, -2, v2
	s_nop 0
	v_cndmask_b32_e32 v51, v197, v51, vcc
	v_cmp_gt_u32_e32 vcc, s71, v16
	v_add_u32_e32 v16, -3, v2
	s_nop 0
	v_cndmask_b32_e32 v52, v197, v52, vcc
	v_cmp_gt_u32_e32 vcc, s71, v16
	v_add_u32_e32 v16, -8, v2
	s_nop 0
	v_cndmask_b32_e32 v53, v197, v53, vcc
	v_cmp_gt_u32_e32 vcc, s71, v16
	v_add_u32_e32 v16, -9, v2
	s_nop 0
	v_cndmask_b32_e32 v54, v197, v54, vcc
	v_cmp_gt_u32_e32 vcc, s71, v16
	v_add_u32_e32 v16, -10, v2
	s_nop 0
	v_cndmask_b32_e32 v55, v197, v55, vcc
	v_cmp_gt_u32_e32 vcc, s71, v16
	v_add_u32_e32 v16, -11, v2
	s_nop 0
	v_cndmask_b32_e32 v56, v197, v56, vcc
	v_cmp_gt_u32_e32 vcc, s71, v16
	v_add_u32_e32 v16, -16, v2
	s_nop 0
	v_cndmask_b32_e32 v57, v197, v57, vcc
	v_cmp_gt_u32_e32 vcc, s71, v16
	v_subrev_u32_e32 v16, 17, v2
	s_nop 0
	v_cndmask_b32_e32 v58, v197, v58, vcc
	v_cmp_gt_u32_e32 vcc, s71, v16
	v_subrev_u32_e32 v16, 18, v2
	s_nop 0
	v_cndmask_b32_e32 v59, v197, v59, vcc
	v_cmp_gt_u32_e32 vcc, s71, v16
	v_subrev_u32_e32 v16, 19, v2
	s_nop 0
	v_cndmask_b32_e32 v60, v197, v60, vcc
	v_cmp_gt_u32_e32 vcc, s71, v16
	v_subrev_u32_e32 v16, 24, v2
	s_nop 0
	v_cndmask_b32_e32 v61, v197, v61, vcc
	v_cmp_gt_u32_e32 vcc, s71, v16
	v_subrev_u32_e32 v16, 25, v2
	s_nop 0
	v_cndmask_b32_e32 v62, v197, v62, vcc
	v_cmp_gt_u32_e32 vcc, s71, v16
	v_subrev_u32_e32 v16, 26, v2
	v_subrev_u32_e32 v2, 27, v2
	v_cndmask_b32_e32 v63, v197, v63, vcc
	v_cmp_gt_u32_e32 vcc, s71, v16
	s_nop 1
	v_cndmask_b32_e32 v64, v197, v64, vcc
	v_cmp_gt_u32_e32 vcc, s71, v2
	s_nop 1
	v_cndmask_b32_e32 v65, v197, v65, vcc
